# in-proj GEMM phase: workgroups de-phased at phase entry by s_sleep (position-in-XCD x ~0.55us) so epilogue store bursts do not coincide
# baseline (speedup 1.0000x reference)
; template <bool PERM, class Epi, class Sched>
; __device__ __forceinline__ void gemm_phase(LAS unsigned char* lds, const Sched& S, const Epi& E) {
;     ...
;     if (GEMM_SKEW_TICKS > 0 && Sched::SKEW) {
;         const unsigned long long t0 = __builtin_amdgcn_s_memrealtime(), w = (unsigned long long)(blockIdx.x & 7u) * (GEMM_SKEW_TICKS);
;         while (__builtin_amdgcn_s_memrealtime() - t0 < w) __builtin_amdgcn_s_sleep(8);
;     }
;     __device__ __forceinline__ bool next(int i, gm::GUnit& u) const {
;         const int L = i * G + c, nlat = 256 * 16, nproj = nlat + (l == 0 ? 8 * 16 : 8 * 4), ngate = (l == 0 ? 264 : 256) * 16;
;         if (L >= nproj + ngate) return false;
;         int pm, pn, sub = 0;
;         if (L < nlat) grouped_order(L, 256, 16, pm, pn);
;         else if (L < nproj) { const int r = L - nlat; if (l == 0) { pm = 256 + (r >> 4); pn = r & 15; } else { pm = 256 + (r >> 2); pn = 2 + (r & 3); } }
;         else { grouped_order(L - nproj, l == 0 ? 264 : 256, 16, pm, pn); sub = 1; }
.LBB0_225:
	v_writelane_b32 v255, s54, 11
	s_andn2_b64 vcc, exec, s[8:9]
	s_nop 0
	v_writelane_b32 v255, s55, 12
	s_cbranch_vccnz .LBB0_318
	v_readlane_b32 s100, v254, 62
	s_nop 3
	s_lshr_b32 s100, s100, 3
	s_and_b32 s100, s100, 31
	s_cmp_eq_u32 s100, 0
	s_cbranch_scc1 .Lskew_done_proj
.Lskew_proj:
	s_sleep 16
	s_sub_u32 s100, s100, 1
	s_cmp_lg_u32 s100, 0
	s_cbranch_scc1 .Lskew_proj
.Lskew_done_proj:
	s_and_b64 s[0:1], s[64:65], exec
	s_movk_i32 s0, 0x2100
	v_mov_b32_e32 v1, v0
	s_cselect_b32 s31, s0, 0x2020
	v_readlane_b32 s0, v254, 62
	s_cmp_ge_i32 s0, s31
	v_readfirstlane_b32 s30, v1
	v_readlane_b32 s1, v254, 63
	s_cbranch_scc1 .LBB0_268
	s_add_u32 s8, s56, 0x916100
	s_addc_u32 s9, s57, 0
	s_and_b64 s[0:1], s[64:65], exec
	s_movk_i32 s0, 0x1080
	s_cselect_b32 s58, s0, 0x1020
	v_readlane_b32 s0, v252, 44
	v_readlane_b32 s1, v252, 45
	s_andn2_b64 vcc, exec, s[0:1]
	s_mov_b32 s0, 0
	s_cbranch_vccnz .LBB0_233
	v_readlane_b32 s0, v254, 62
	s_cmp_ge_u32 s0, s58
	s_mov_b64 s[22:23], -1
	v_readlane_b32 s1, v254, 63
	s_cbranch_scc0 .LBB0_230
	s_add_u32 s18, s56, 0x1916100
	v_readlane_b32 s0, v254, 62
	s_addc_u32 s19, s57, 0
	v_readlane_b32 s1, v254, 63
	s_sub_i32 s2, s0, s58
	s_and_b64 s[0:1], s[64:65], exec
	s_movk_i32 s0, 0x108
	s_cselect_b32 s0, s0, 0x100
	v_readlane_b32 s1, v252, 46
	s_mul_i32 s1, s0, s1
	s_lshr_b32 s2, s2, 3
	s_add_i32 s2, s2, s1
	s_lshr_b32 s1, s2, 4
	s_and_b32 s7, s1, 0x1fffff8
	s_sub_i32 s0, s0, s7
	s_min_i32 s22, s0, 8
	s_sext_i32_i8 s0, s22
	s_waitcnt vmcnt(0)
	v_cvt_f32_i32_e32 v2, s0
	s_and_b32 s2, s2, 0x7f
	v_cvt_f32_ubyte0_e32 v4, s2
	s_ashr_i32 s0, s0, 30
	v_rcp_iflag_f32_e32 v3, v2
	s_or_b32 s23, s0, 1
	v_mul_f32_e32 v3, v4, v3
	v_trunc_f32_e32 v3, v3
	v_fma_f32 v4, -v3, v2, v4
	v_cvt_i32_f32_e32 v3, v3
	v_cmp_ge_f32_e64 s[0:1], |v4|, |v2|
	s_and_b64 s[0:1], s[0:1], exec
	s_cselect_b32 s0, s23, 0
	v_readfirstlane_b32 s1, v3
	s_add_i32 s0, s1, s0
	s_sext_i32_i8 s74, s0
	s_mul_i32 s0, s0, s22
	s_sub_i32 s0, s2, s0
	s_and_b32 s0, s0, 0xff
	s_add_i32 s72, s7, s0
	s_mov_b64 s[22:23], 0

; __global__ void __launch_bounds__(NTHR, 2) fwd_kernel(Params prm) {
	.amdhsa_kernel _Z10fwd_kernel6Params
		.amdhsa_group_segment_fixed_size 0
		.amdhsa_private_segment_fixed_size 0
		.amdhsa_kernarg_size 496
		.amdhsa_user_sgpr_count 2
		.amdhsa_user_sgpr_dispatch_ptr 0
		.amdhsa_user_sgpr_queue_ptr 0
		.amdhsa_user_sgpr_kernarg_segment_ptr 1
		.amdhsa_user_sgpr_dispatch_id 0
		.amdhsa_user_sgpr_kernarg_preload_length 0
		.amdhsa_user_sgpr_kernarg_preload_offset 0
		.amdhsa_user_sgpr_private_segment_size 0
		.amdhsa_uses_dynamic_stack 0
		.amdhsa_enable_private_segment 0
		.amdhsa_system_sgpr_workgroup_id_x 1
		.amdhsa_system_sgpr_workgroup_id_y 0
		.amdhsa_system_sgpr_workgroup_id_z 0
		.amdhsa_system_sgpr_workgroup_info 0
		.amdhsa_system_vgpr_workitem_id 0
		.amdhsa_next_free_vgpr 256
		.amdhsa_next_free_sgpr 102
		.amdhsa_accum_offset 256
		.amdhsa_reserve_vcc 1
		.amdhsa_float_round_mode_32 0
		.amdhsa_float_round_mode_16_64 0
		.amdhsa_float_denorm_mode_32 3
		.amdhsa_float_denorm_mode_16_64 3
		.amdhsa_dx10_clamp 1
		.amdhsa_ieee_mode 1
		.amdhsa_fp16_overflow 0
		.amdhsa_tg_split 0
		.amdhsa_exception_fp_ieee_invalid_op 0
		.amdhsa_exception_fp_denorm_src 0
		.amdhsa_exception_fp_ieee_div_zero 0
		.amdhsa_exception_fp_ieee_overflow 0
		.amdhsa_exception_fp_ieee_underflow 0
		.amdhsa_exception_fp_ieee_inexact 0
		.amdhsa_exception_int_div_zero 0
	.end_amdhsa_kernel

; __global__ void __launch_bounds__(NTHR, 2) fwd_kernel(Params prm) {
amdhsa.kernels:
  - .agpr_count:     0
    .args:
      - .offset:         0
        .size:           240
        .value_kind:     by_value
      - .offset:         240
        .size:           4
        .value_kind:     hidden_block_count_x
      - .offset:         244
        .size:           4
        .value_kind:     hidden_block_count_y
      - .offset:         248
        .size:           4
        .value_kind:     hidden_block_count_z
      - .offset:         252
        .size:           2
        .value_kind:     hidden_group_size_x
      - .offset:         254
        .size:           2
        .value_kind:     hidden_group_size_y
      - .offset:         256
        .size:           2
        .value_kind:     hidden_group_size_z
      - .offset:         258
        .size:           2
        .value_kind:     hidden_remainder_x
      - .offset:         260
        .size:           2
        .value_kind:     hidden_remainder_y
      - .offset:         262
        .size:           2
        .value_kind:     hidden_remainder_z
      - .offset:         280
        .size:           8
        .value_kind:     hidden_global_offset_x
      - .offset:         288
        .size:           8
        .value_kind:     hidden_global_offset_y
      - .offset:         296
        .size:           8
        .value_kind:     hidden_global_offset_z
      - .offset:         304
        .size:           2
        .value_kind:     hidden_grid_dims
      - .offset:         360
        .size:           4
        .value_kind:     hidden_dynamic_lds_size
    .group_segment_fixed_size: 0
    .kernarg_segment_align: 8
    .kernarg_segment_size: 496
    .language:       OpenCL C
    .language_version:
      - 2
      - 0
    .max_flat_workgroup_size: 512
    .name:           _Z10fwd_kernel6Params
    .private_segment_fixed_size: 0
    .sgpr_count:     108
    .sgpr_spill_count: 221
    .symbol:         _Z10fwd_kernel6Params.kd
    .uniform_work_group_size: 1
    .uses_dynamic_stack: false
    .vgpr_count:     256
    .vgpr_spill_count: 0
    .wavefront_size: 64
